# v31
# baseline (speedup 1.0000x reference)
.LBB2_31:
	s_add_i32 s17, s17, 3
	s_ashr_i32 s2, s17, 2
	v_subrev_u32_e32 v8, s6, v8
	s_max_i32 s6, s2, 1
	s_setprio 0
	s_add_i32 s2, s4, s7
	s_add_i32 s2, s2, s16
	s_add_i32 s2, s2, s6
	s_add_i32 s2, s2, -1
	s_lshr_b32 s22, s2, 1
	v_mov_b32_e32 v45, 0
	s_mov_b32 s2, 0x3a800000
	s_mov_b32 s17, 0
	s_mov_b32 s23, 0xc040c00
	s_mov_b32 s24, 0xc050c01
	s_mov_b32 s25, 0xc060c02
	s_mov_b32 s26, 0xc070c03
	s_mov_b32 s3, 0xc3000000
	v_mov_b32_e32 v9, 0x186a0
	s_mov_b32 s5, 0
	v_mov_b32_e32 v60, 0
	v_mov_b32_e32 v42, v45
	v_mov_b32_e32 v43, v45
	v_mov_b32_e32 v36, v45
	v_mov_b32_e32 v37, v45
	v_mov_b32_e32 v30, v45
	v_mov_b32_e32 v31, v45
	v_mov_b32_e32 v53, 0
	s_branch .LBB2_35
	s_nop 0
	s_nop 0
	s_nop 0
	s_nop 0
	s_nop 0
	s_nop 0
	s_nop 0

.LBB2_107:
	s_or_b64 exec, exec, s[2:3]
	s_load_dwordx4 s[4:7], s[0:1], 0x38
	s_cmpk_lt_i32 s19, 0x181
	s_cbranch_scc0 .LBB2_62
	s_branch .LBB2_63
	s_nop 0
	s_nop 0
	s_nop 0
	s_nop 0
	s_nop 0
	s_nop 0
	s_nop 0
	s_nop 0
	s_nop 0
	s_nop 0
	s_nop 0
	s_nop 0
	s_nop 0
	s_nop 0
	s_nop 0
	s_nop 0
	s_nop 0
	s_nop 0
	s_nop 0
	s_nop 0
	s_nop 0
	s_nop 0
	s_nop 0
	s_nop 0
	s_nop 0
	s_nop 0
	s_nop 0
	s_nop 0
	s_nop 0
	s_nop 0
	s_nop 0
	s_nop 0
	s_nop 0
	s_nop 0
	s_nop 0
	s_nop 0
	s_nop 0
	s_nop 0
	s_nop 0
	s_nop 0
	s_nop 0
	s_nop 0
	s_nop 0
	s_nop 0
	s_nop 0
	s_nop 0
	s_nop 0
	s_nop 0
	s_nop 0
	s_nop 0
	s_nop 0
	s_nop 0
	s_nop 0
	s_nop 0
	s_nop 0
	s_nop 0
	s_nop 0
	s_nop 0
	s_nop 0
	s_nop 0
	s_endpgm

.LBB3_29:
	s_add_i32 s18, s18, 3
	s_ashr_i32 s2, s18, 2
	v_subrev_u32_e32 v7, s6, v7
	s_max_i32 s6, s2, 1
	s_setprio 0
	s_add_i32 s2, s4, s14
	s_add_i32 s2, s2, s15
	s_add_i32 s2, s2, s6
	s_add_i32 s2, s2, -1
	s_lshr_b32 s20, s2, 1
	v_mov_b32_e32 v45, 0
	s_mov_b32 s2, 0x3a800000
	s_mov_b32 s18, 0
	s_mov_b32 s21, 0xc040c00
	s_mov_b32 s22, 0xc050c01
	s_mov_b32 s23, 0xc060c02
	s_mov_b32 s24, 0xc070c03
	s_brev_b32 s3, 1
	v_mov_b32_e32 v8, 0x186a0
	s_mov_b32 s5, 0
	v_mov_b32_e32 v56, 0
	v_mov_b32_e32 v42, v45
	v_mov_b32_e32 v43, v45
	v_mov_b32_e32 v36, v45
	v_mov_b32_e32 v37, v45
	v_mov_b32_e32 v30, v45
	v_mov_b32_e32 v31, v45
	v_mov_b32_e32 v49, 0
	s_branch .LBB3_33
	s_nop 0
	s_nop 0
	s_nop 0
	s_nop 0
	s_nop 0
	s_nop 0
	s_nop 0
	s_nop 0
	s_nop 0
	s_nop 0
	s_nop 0
